# 2 (instead of 3) weight-conversion items per wave left for the top-k phase (one more item per wave converted beside the input projection)
# speedup vs baseline: 1.0038x; 1.0038x over previous
.LBB0_265:
	v_readlane_b32 s12, v235, 0
	v_readlane_b32 s14, v235, 2
	s_cmp_lt_i32 s16, s27
	s_cselect_b64 s[8:9], -1, 0
	s_cmp_eq_u32 s27, s14
	v_readlane_b32 s13, v235, 1
	s_cselect_b64 s[2:3], -1, 0
	s_cmp_lg_u32 s27, s14
	s_cselect_b64 s[12:13], -1, 0
	s_and_b64 s[8:9], s[8:9], s[12:13]
	s_mul_i32 s52, s14, 0xfffffff0
	s_and_b64 vcc, exec, s[8:9]
	v_readlane_b32 s15, v235, 3
	s_cbranch_vccnz .LBB0_293
	s_add_i32 s8, s52, 0x8600
	s_and_b64 s[0:1], s[0:1], exec
	s_cselect_b32 s53, s8, 0x8400
	s_and_b64 s[0:1], s[2:3], exec
	v_readlane_b32 s0, v235, 16
	s_cselect_b32 s34, 0, s27
	v_readlane_b32 s1, v235, 17
	v_mov_b32_e32 v64, v186
	s_sub_i32 s0, s0, s34
	s_lshl_b32 s0, s0, 3
	v_readfirstlane_b32 s1, v64
	s_ashr_i32 s35, s1, 6
	s_add_i32 s16, s35, s0
	s_cmp_ge_i32 s16, s53
	s_cbranch_scc1 .LBB0_293
	s_mul_hi_i32 s12, s16, 0x3e0f83e1
	s_lshr_b32 s13, s12, 31
	s_ashr_i32 s22, s12, 9
	s_add_i32 s22, s22, s13
	s_mul_i32 s12, s22, 0xfffff7c0
	s_add_i32 s17, s12, s16
	s_add_i32 s12, s17, 0xfffffd40
	s_cmpk_lt_u32 s12, 0x2c0
	s_cselect_b64 s[12:13], -1, 0
	s_and_b64 s[14:15], s[12:13], exec
	s_load_dwordx4 s[0:3], s[10:11], 0x70
	s_load_dwordx2 s[8:9], s[10:11], 0x80
	s_cselect_b32 s18, 0xfffffd40, 0
	s_cmpk_lt_i32 s17, 0x580
	s_cselect_b64 s[14:15], -1, 0
	s_and_b64 vcc, exec, s[14:15]
	s_cselect_b32 s20, s18, 0xfffffa80
	s_add_i32 s20, s20, s17
	s_cbranch_vccnz .LBB0_269
	s_and_b32 s30, s16, 31
	s_ashr_i32 s31, s20, 5
	s_waitcnt lgkmcnt(0)
	s_mov_b64 s[16:17], s[8:9]
	s_load_dwordx2 s[10:11], s[10:11], 0x98
	s_cbranch_execz .LBB0_270
	s_branch .LBB0_271

.LBB0_712:
	s_or_b64 exec, exec, s[0:1]
	v_readlane_b32 s0, v235, 0
	v_readlane_b32 s2, v235, 2
	v_readlane_b32 s3, v235, 3
	v_readlane_b32 s1, v235, 1
	s_cmp_gt_i32 s2, 63
	v_readlane_b32 s2, v235, 16
	s_cselect_b64 s[0:1], -1, 0
	s_cmp_lt_i32 s2, 32
	v_readlane_b32 s3, v235, 17
	s_cselect_b64 s[4:5], -1, 0
	s_cmp_gt_i32 s2, 31
	s_cselect_b64 s[2:3], -1, 0
	s_and_b64 s[2:3], s[2:3], s[0:1]
	s_mov_b64 s[6:7], s[46:47]
	s_mov_b64 s[0:1], -1
	s_and_b64 vcc, exec, s[2:3]
	v_readlane_b32 s46, v235, 10
	s_waitcnt lgkmcnt(0)
	s_barrier
	v_readlane_b32 s47, v235, 11
	s_cbranch_vccz .LBB0_724
	v_readlane_b32 s0, v235, 12
	v_readlane_b32 s1, v235, 13
	v_mov_b32_e32 v0, v186
	s_add_i32 s0, s52, s0
	v_readfirstlane_b32 s1, v0
	s_ashr_i32 s12, s1, 6
	s_add_i32 s0, s0, s12
	s_add_i32 s30, s0, 0x8500
	s_cmp_gt_i32 s30, 0x83ff
	s_cbranch_scc1 .LBB0_723
	s_load_dwordx4 s[0:3], s[6:7], 0x70
	s_load_dwordx2 s[8:9], s[6:7], 0x80
	s_load_dwordx2 s[10:11], s[6:7], 0x98
	s_mulk_i32 s12, 0x2100
	v_bfe_u32 v12, v0, 1, 5
	v_lshlrev_b32_e32 v1, 2, v0
	v_bfe_u32 v14, v0, 3, 3
	v_and_b32_e32 v0, 7, v0
	s_add_i32 s12, s12, 0
	v_and_b32_e32 v2, 28, v1
	v_mul_u32_u24_e32 v1, 0x220, v0
	v_lshlrev_b32_e32 v3, 2, v14
	v_lshlrev_b32_e32 v8, 4, v0
	v_add3_u32 v15, s12, v1, v3
	v_add_u32_e32 v0, s12, v8
	v_mul_u32_u24_e32 v1, 0x88, v14
	v_mov_b32_e32 v9, 0
	v_add_u32_e32 v20, v0, v1
	s_add_i32 s31, s46, 0xffffff00
	s_mov_b32 s13, 0
	v_and_b32_e32 v13, 28, v12
	v_or_b32_e32 v16, 8, v14
	v_or_b32_e32 v17, 16, v14
	v_or_b32_e32 v18, 24, v14
	v_lshlrev_b32_e32 v10, 2, v2
	v_mov_b32_e32 v11, v9
	s_mov_b32 s33, 0xc3e00000
	v_mov_b32_e32 v19, 0x43e00000
	v_add_u32_e32 v21, 0x880, v20
	v_add_u32_e32 v22, 0xcc0, v20
	s_branch .LBB0_717
